# adds: P2 queue pop no longer drains the finished unit's stores before the atomic and after the item broadcast (later counted waits cover them)
# baseline (speedup 1.0000x reference)
; __device__ void phase2(const Params& p, unsigned char* smem, unsigned* qw) {
;     ...
;     for (;;) {
;         const bool take_conv = conv_left && (conv_first || !att_left);
;         if (!take_conv && !att_left) break;
;         const int q = (x + aq) & 7;
;         __syncthreads();
;         if (threadIdx.x == 0) *qslot = (int)__hip_atomic_fetch_add(qw + (take_conv ? 0 : 64 * (2 + q)), 1u, __ATOMIC_RELAXED, __HIP_MEMORY_SCOPE_AGENT);
;         __syncthreads();
;         const int item = *qslot;
.LBB0_373:
	s_add_i32 s22, s85, s2
	s_and_b32 s5, s22, 7
	s_barrier
	s_and_saveexec_b64 s[6:7], s[72:73]
	s_cbranch_execz .LBB0_377
	s_mov_b64 s[10:11], exec
	v_mbcnt_lo_u32_b32 v2, s10, 0
	v_mbcnt_hi_u32_b32 v2, s11, v2
	v_cmp_eq_u32_e32 vcc, 0, v2
	s_and_saveexec_b64 s[8:9], vcc
	s_cbranch_execz .LBB0_376
	s_lshl_b32 s4, s5, 6
	s_addk_i32 s4, 0x80
	s_and_b64 s[12:13], s[0:1], exec
	s_cselect_b32 s4, 0, s4
	s_bcnt1_i32_b64 s10, s[10:11]
	s_lshl_b32 s4, s4, 2
	v_mov_b32_e32 v4, s10
	v_readlane_b32 s10, v248, 13
	v_mov_b32_e32 v3, s4
	v_readlane_b32 s11, v248, 14
	s_nop 4
	global_atomic_add v3, v3, v4, s[10:11] sc0

; template <bool ISA>
; __device__ __forceinline__ void attn_unit(const Params& p, unsigned char* smem, int b, int hh, int blk) {
;     ...
;     const int tid = otid() & 255, lane = tid & 63, wid = tid >> 6, l15 = lane & 15, gq = lane >> 4;
;     int nl, tbase;
;     if (ISA) {
;         const int start = blk * 128;
;         const int j0 = start >= 128 ? 0 : 2, j1 = (start + 256 <= SEQ) ? 6 : 4;
;         nl = j1 - j0; tbase = start - 128 + 64 * j0;
;     } else {
;         int rs = 2 * blk - 4; rs = rs < 0 ? 0 : (rs > 119 ? 119 : rs);
;         nl = 9; tbase = rs * 64;
;     }
;     const int ntile = nl + 4;
;     const bf16_t* kbase; const bf16_t* vbase; int ldk;
;     if (ISA) { const int g = hh >> 2; kbase = p.ka + (size_t)(b * TT) * 128 + g * 64; ldk = 128; vbase = p.vta + (size_t)((b * 2 + g) * 64) * TT; }
;     else { kbase = p.kb + (size_t)(b * TT) * 512 + hh * 64; ldk = 512; vbase = p.vtb + (size_t)((b * 8 + hh) * 64) * TT; }
;     float* rpbl = (float*)(smem + 49152);
;     const float M2 = p.attm[ISA ? hh : 8 + hh], negM2 = -M2;
;     const int qt0 = ISA ? blk * 128 + wid * 32 : blk * 128 + wid * 16;
;     bf16x8 qf[NQ][2];
;     {
;         const bf16_t* qsrc = ISA ? p.qa : p.qb;
; #pragma unroll
;         for (int q = 0; q < NQ; ++q)
; #pragma unroll
;             for (int ks = 0; ks < 2; ++ks)
;                 qf[q][ks] = *(const bf16x8*)(qsrc + (size_t)(b * TT + qt0 + q * QSTR + l15) * 512 + hh * 64 + ks * 32 + gq * 8);
;     }
;     f32x4 osum[NQ]; f32x4 o[NQ][4];
; #pragma unroll
;     for (int q = 0; q < NQ; ++q) {
;         const float l0 = ISA ? __builtin_amdgcn_exp2f(p.sink[hh] * L2E - M2) : 0.f;
;         osum[q] = (f32x4){l0, l0, l0, l0};
; #pragma unroll
; __device__ void phase2(const Params& p, unsigned char* smem, unsigned* qw) {
;     ...
;         const int item = *qslot;
;         if (take_conv) {
;             if (item >= nchunks) { conv_left = false; continue; }
;             conv_jobs_deep(p, smem, item * 16, item * 16 + 16);
;         } else {
;             if (item >= 256) { if (++aq == 8) att_left = false; continue; }
;             if (item < 128) {
;                 const int u = item * 2 + sub;
;                 attn_unit<true>(p, sm, q >> 1, (q & 1) * 4 + (u & 3), u >> 2);
;             } else {
;                 const int j = item - 128;
;                 attn_unit<false>(p, sm, j >> 5, q, (j & 31) * 2 + sub);
.LBB0_377:
	s_or_b64 exec, exec, s[6:7]
	s_waitcnt lgkmcnt(0)
	s_barrier
	ds_read_b32 v2, v118
	s_xor_b64 s[6:7], s[0:1], -1
	s_mov_b64 s[0:1], -1
	s_and_b64 vcc, exec, s[6:7]
	s_waitcnt lgkmcnt(0)
	v_readfirstlane_b32 s4, v2
	s_cbranch_vccz .LBB0_429
	s_cmpk_lt_i32 s4, 0x100
	s_cbranch_scc0 .LBB0_426
	s_cmpk_gt_i32 s4, 0x7f
	s_cbranch_scc0 .LBB0_401
	s_add_i32 s0, s4, 0xffffff80
	s_lshr_b32 s24, s0, 5
	s_lshl_b32 s76, s5, 6
	s_lshl_b32 s6, s24, 9
	s_lshl_b32 s0, s4, 1
	s_or_b32 s6, s6, s76
	s_and_b32 s0, s0, 62
	s_mulk_i32 s6, 0x2100
	s_mov_b32 s7, s77
	v_add_u32_e32 v21, s0, v1
	v_mov_b32_e32 v30, v0
	s_lshl_b64 s[6:7], s[6:7], 1
	v_readlane_b32 s9, v248, 26
	v_lshlrev_b32_e32 v101, 1, v21
	v_bfe_u32 v31, v30, 6, 2
	s_add_u32 s6, s9, s6
	v_readlane_b32 s9, v248, 28
	v_add_u32_e32 v19, -4, v101
	s_addc_u32 s7, s9, s7
	s_or_b32 s23, s5, 8
	v_lshlrev_b32_e32 v20, 4, v31
	v_min_i32_e32 v2, 0x77, v19
	s_mul_i32 s8, s24, 0x2100
	s_lshl_b32 s9, s23, 2
	v_lshl_or_b32 v100, v21, 7, v20
	v_lshlrev_b32_e32 v22, 6, v2
	v_mov_b32_e32 v4, s9
	v_add_u32_e32 v2, s8, v100
	s_lshl_b32 s10, s5, 7
	v_readlane_b32 s8, v248, 9
	v_and_b32_e32 v112, 15, v30
	v_readlane_b32 s9, v248, 10
	s_add_u32 s8, s8, s10
	v_or_b32_e32 v6, v2, v112
	s_addc_u32 s9, s9, 0
	v_and_b32_e32 v98, 48, v30
	v_lshl_add_u64 v[8:9], s[8:9], 0, v[98:99]
	v_ashrrev_i32_e32 v7, 31, v6
	v_readlane_b32 s8, v248, 20
	s_mul_i32 s0, s24, 0x420000
	s_mov_b32 s1, s77
	v_lshlrev_b64 v[2:3], 10, v[6:7]
	v_readlane_b32 s9, v248, 21
	v_lshl_add_u64 v[10:11], v[8:9], 0, v[2:3]
	s_nop 3
	global_load_dword v113, v4, s[8:9]
	s_nop 0
	global_load_dwordx4 v[2:5], v[10:11], off
	s_lshl_b64 s[0:1], s[0:1], 1
	v_readlane_b32 s8, v248, 7
	v_readlane_b32 s9, v248, 8
	s_add_u32 s0, s8, s0
	v_cmp_gt_i32_e32 vcc, 2, v21
	v_bfe_u32 v21, v30, 3, 3
	s_addc_u32 s1, s9, s1
	v_or_b32_e32 v21, v20, v21
	v_bfe_u32 v18, v30, 4, 2
	s_add_u32 s0, s0, s10
	v_or_b32_e32 v28, 8, v21
	s_addc_u32 s1, s1, 0
	v_cndmask_b32_e64 v102, v22, 0, vcc
	v_bitop3_b32 v24, v18, v30, 7 bitop3:0x78
	v_lshrrev_b32_e32 v22, 1, v28
	v_lshlrev_b32_e32 v98, 10, v21
	v_xor_b32_e32 v25, v22, v30
	v_lshl_add_u64 v[22:23], s[0:1], 0, v[98:99]
	v_lshlrev_b32_e32 v98, 4, v24
	v_lshl_add_u64 v[104:105], v[22:23], 0, v[98:99]
	v_lshlrev_b32_e32 v22, 10, v28
	v_mov_b32_e32 v23, v99
	v_lshlrev_b32_e32 v24, 4, v25
	v_or_b32_e32 v6, 64, v6
	v_readfirstlane_b32 s8, v31
	v_lshl_add_u64 v[22:23], s[0:1], 0, v[22:23]
	v_and_b32_e32 v24, 0x70, v24
	v_mov_b32_e32 v25, v99
	v_ashrrev_i32_e32 v7, 31, v6
	v_lshl_add_u64 v[106:107], v[22:23], 0, v[24:25]
	v_mov_b64_e32 v[22:23], s[6:7]
	s_movk_i32 s6, 0x4200
	s_lshl_b32 s25, s8, 11
	v_lshlrev_b64 v[6:7], 10, v[6:7]
	v_mad_u64_u32 v[26:27], s[0:1], v21, s6, v[22:23]
	v_mad_u64_u32 v[22:23], s[0:1], v28, s6, v[22:23]
	v_ashrrev_i32_e32 v103, 31, v102
	v_add_u32_e32 v21, s25, v114
	v_lshl_add_u64 v[14:15], v[8:9], 0, v[6:7]
	v_lshl_add_u64 v[108:109], v[26:27], 0, v[98:99]
	v_lshl_add_u64 v[110:111], v[22:23], 0, v[24:25]
	v_lshlrev_b64 v[22:23], 10, v[102:103]
	v_readfirstlane_b32 s0, v21
	v_add_u32_e32 v26, 0x400, v21
	global_load_dwordx4 v[6:9], v[10:11], off offset:64
	s_nop 0
	global_load_dwordx4 v[10:13], v[14:15], off
	s_nop 0
	global_load_dwordx4 v[14:17], v[14:15], off offset:64
	s_waitcnt lgkmcnt(0)
	s_barrier
; #define LAS __attribute__((address_space(3)))
; template <bool ISA>
; __device__ __forceinline__ void attn_unit(const Params& p, unsigned char* smem, int b, int hh, int blk) {
;     ...
;     const int qcol = wid * 16 + l15;
;     int cs = wid * 16 - 8; cs = cs < 0 ? 0 : (cs > 32 ? 32 : cs);
;     int wstart = qcol - 8; wstart = wstart < 0 ? 0 : (wstart > 48 ? 48 : wstart);
;     NaConst nc;
; #pragma unroll
;     for (int j = 0; j < 4; ++j) {
;         const int kc = cs + (j >> 1) * 16 + gq * 4 + (j & 1) * 2;
;         nc.cm[j] = (((kc >= wstart) && (kc < wstart + 16)) ? 0xFFFFu : 0u) | (((kc + 1 >= wstart) && (kc + 1 < wstart + 16)) ? 0xFFFF0000u : 0u);
;     }
;     nc.blane = (unsigned)(size_t)(LAS unsigned char*)smem + 49152u + (unsigned)((16 + (cs + gq * 4 - qcol + 15)) * 4);
;     LAS unsigned char* ldsu = (LAS unsigned char*)smem;
;     const unsigned ldsa = (unsigned)(size_t)ldsu;
;     const int wuni = __builtin_amdgcn_readfirstlane(wid);
;     const bf16_t* kp0; const bf16_t* kp1; const bf16_t* vp0; const bf16_t* vp1;
;     {
;         const int ra = (wid * 2) * 8 + (lane >> 3), rb = (wid * 2 + 1) * 8 + (lane >> 3);
;         const int ca = ((lane & 7) ^ ((ra >> 1) & 7)) * 8, cb = ((lane & 7) ^ ((rb >> 1) & 7)) * 8;
;         kp0 = kbase + (size_t)ra * ldk + ca; kp1 = kbase + (size_t)rb * ldk + cb;
;         vp0 = vbase + (size_t)ra * TT + ca; vp1 = vbase + (size_t)rb * TT + cb;
;     }
;     ...
;     asm volatile("s_waitcnt lgkmcnt(0)" ::: "memory"); __builtin_amdgcn_s_barrier(); asm volatile("" ::: "memory");
;     ADMA(0);
;     if (ntile > 1) ADMA(1);
;     if (!ISA) {
;         for (int i = tid; i < 15 * 64; i += 256) { const int dr = i >> 6, dc = (i & 63) - 16; rpbl[i] = ((dc >= 0 && dc < 31) ? p.rpb[hh * 465 + dr * 31 + dc] * L2E : 0.f) - M2; }
	v_lshl_add_u64 v[24:25], v[104:105], 0, v[22:23]
	s_mov_b32 m0, s0
	v_readfirstlane_b32 s0, v26
	global_load_lds_dwordx4 v[24:25], off
	v_lshl_add_u64 v[24:25], v[106:107], 0, v[22:23]
	s_mov_b32 m0, s0
	v_add_u32_e32 v28, 0x6000, v21
	global_load_lds_dwordx4 v[24:25], off
	v_lshlrev_b64 v[24:25], 1, v[102:103]
	v_readfirstlane_b32 s0, v28
	v_add_u32_e32 v28, 0x6400, v21
	v_lshl_add_u64 v[26:27], v[108:109], 0, v[24:25]
	s_mov_b32 m0, s0
	v_readfirstlane_b32 s0, v28
	global_load_lds_dwordx4 v[26:27], off
	s_mov_b32 m0, s0
	s_mov_b64 s[0:1], 0x10000
	v_add_u32_e32 v32, 0x2000, v21
	v_lshl_add_u64 v[24:25], v[110:111], 0, v[24:25]
	v_lshl_add_u64 v[22:23], v[22:23], 0, s[0:1]
	v_readfirstlane_b32 s0, v32
	global_load_lds_dwordx4 v[24:25], off
	v_lshl_add_u64 v[28:29], v[104:105], 0, v[22:23]
	s_mov_b32 m0, s0
	v_lshl_add_u64 v[22:23], v[106:107], 0, v[22:23]
	global_load_lds_dwordx4 v[28:29], off
	v_add_u32_e32 v28, 0x2400, v21
	s_mov_b64 s[6:7], 0x80
	v_readfirstlane_b32 s0, v28
	s_mov_b32 m0, s0
	v_and_b32_e32 v103, 63, v30
	global_load_lds_dwordx4 v[22:23], off
	v_lshl_add_u64 v[22:23], v[26:27], 0, s[6:7]
	v_add_u32_e32 v26, 0x8000, v21
	v_add_u32_e32 v21, 0x8400, v21
	v_readfirstlane_b32 s0, v26
	s_mov_b32 m0, s0
	v_readfirstlane_b32 s0, v21
	global_load_lds_dwordx4 v[22:23], off
	v_lshl_add_u64 v[22:23], v[24:25], 0, s[6:7]
	s_mov_b32 m0, s0
	s_mul_i32 s6, s5, 0x1d1
	global_load_lds_dwordx4 v[22:23], off
	v_and_b32_e32 v23, 0xff, v30
	v_add_u32_e32 v22, -16, v103
	s_add_i32 s6, s6, -16
	v_mul_u32_u24_e32 v24, 31, v31
	v_lshlrev_b32_e32 v21, 3, v18
	v_cmp_gt_u32_e64 s[0:1], 31, v22
	v_lshl_add_u32 v22, v23, 2, v117
	v_add3_u32 v98, s6, v24, v103
	v_or_b32_e32 v23, 0xffffff00, v23
	v_mov_b32_e32 v26, 0
	v_mov_b32_e32 v27, 0
	v_mov_b32_e32 v28, 0
	v_mov_b32_e32 v29, 0
	v_and_b32_e32 v32, 0xff, v30
	s_movk_i32 s8, 0xc0
	v_lshl_add_u64 v[24:25], v[98:99], 2, s[80:81]
	v_cmp_gt_u32_e64 s[8:9], s8, v32
	s_and_saveexec_b64 s[6:7], s[0:1]
	global_load_dword v26, v[24:25], off
	global_load_dword v27, v[24:25], off offset:496
	global_load_dword v28, v[24:25], off offset:992
	s_and_b64 exec, exec, s[8:9]
	global_load_dword v29, v[24:25], off offset:1488
	s_mov_b64 exec, s[6:7]
	s_waitcnt vmcnt(0)
	v_mul_f32_e32 v26, 0x3fb8aa3b, v26
	v_mul_f32_e32 v27, 0x3fb8aa3b, v27
	v_mul_f32_e32 v28, 0x3fb8aa3b, v28
	v_mul_f32_e32 v29, 0x3fb8aa3b, v29
	v_sub_f32_e32 v26, v26, v113
	v_sub_f32_e32 v27, v27, v113
	v_sub_f32_e32 v28, v28, v113
	v_sub_f32_e32 v29, v29, v113
	ds_write_b32 v22, v26
	ds_write_b32 v22, v27 offset:1024
	ds_write_b32 v22, v28 offset:2048
	s_and_saveexec_b64 s[6:7], s[8:9]
	ds_write_b32 v22, v29 offset:3072
	s_or_b64 exec, exec, s[6:7]
	v_or_b32_e32 v22, v20, v112
	v_med3_u32 v20, v20, 8, 40
	v_add_u32_e32 v20, -8, v20
	v_med3_u32 v23, v22, 8, 56
	v_lshlrev_b32_e32 v98, 2, v18
	v_add_u32_e32 v24, v20, v98
	v_add_u32_e32 v25, 8, v23
	v_add_u32_e32 v23, -8, v23
	v_cmp_lt_u32_e64 s[0:1], v24, v25
	v_or_b32_e32 v26, 1, v24
	v_cmp_ge_u32_e64 s[20:21], v24, v23
	v_cmp_lt_u32_e64 s[6:7], v26, v25
	v_add_u32_e32 v29, 16, v24
	s_and_b64 s[0:1], s[20:21], s[0:1]
	v_cmp_ge_u32_e64 s[20:21], v26, v23
	v_or_b32_e32 v27, 2, v24
	v_or_b32_e32 v28, 3, v24
	v_add_u32_e32 v30, 17, v24
	v_or_b32_e32 v31, 2, v29
	v_add_u32_e32 v32, 19, v24
	s_and_b64 s[6:7], s[20:21], s[6:7]
	v_cmp_lt_u32_e64 s[8:9], v27, v25
	v_cmp_lt_u32_e64 s[10:11], v28, v25
	v_cmp_lt_u32_e64 s[12:13], v29, v25
	v_cmp_lt_u32_e64 s[14:15], v30, v25
	v_cmp_lt_u32_e64 s[16:17], v31, v25
	v_cmp_lt_u32_e64 s[18:19], v32, v25
	v_cndmask_b32_e64 v25, 0, v119, s[6:7]
	v_cmp_ge_u32_e64 s[6:7], v27, v23
	s_and_b64 s[6:7], s[6:7], s[8:9]
	v_cmp_ge_u32_e64 s[8:9], v28, v23
	s_and_b64 s[8:9], s[8:9], s[10:11]
	v_cmp_ge_u32_e64 s[10:11], v30, v23
	v_cndmask_b32_e64 v26, 0, v119, s[8:9]
	v_cmp_ge_u32_e64 s[8:9], v29, v23
	s_and_b64 s[10:11], s[10:11], s[14:15]
	v_cndmask_b32_e64 v28, 0, v120, s[0:1]
	s_and_b64 s[8:9], s[8:9], s[12:13]
	v_cndmask_b32_e64 v27, 0, v119, s[10:11]
	v_cmp_ge_u32_e64 s[10:11], v31, v23
	v_cmp_ge_u32_e64 s[12:13], v32, v23
	v_or_b32_e32 v125, v25, v28
	v_cndmask_b32_e64 v25, 0, v120, s[6:7]
	v_sub_u32_e32 v22, v24, v22
	s_and_b64 s[10:11], s[10:11], s[16:17]
	s_and_b64 s[12:13], s[12:13], s[18:19]
	v_or_b32_e32 v126, v26, v25
	v_cndmask_b32_e64 v25, 0, v120, s[8:9]
	v_min_i32_e32 v19, 0x78, v19
	v_cndmask_b32_e64 v23, 0, v119, s[12:13]
	v_or_b32_e32 v127, v27, v25
	v_cndmask_b32_e64 v25, 0, v120, s[10:11]
	v_lshl_add_u32 v129, v22, 2, v115
	v_lshrrev_b32_e32 v22, 1, v112
	v_cndmask_b32_e64 v137, v19, 0, vcc
	v_med3_i32 v19, v101, 3, v121
	v_or_b32_e32 v128, v25, v23
	v_xor_b32_e32 v25, v18, v22
	v_add_u32_e32 v138, -3, v19
	v_add_u32_e32 v140, 5, v19
	v_add_u16_e32 v19, v20, v112
	v_lshlrev_b32_e32 v131, 4, v25
	v_bitop3_b32 v25, v18, v22, 4 bitop3:0x36
	v_lshrrev_b16_e32 v19, 1, v19
	v_or_b32_e32 v23, 4, v18
	v_lshlrev_b32_e32 v132, 4, v25
	v_lshrrev_b32_e32 v25, 5, v103
	v_bitop3_b32 v18, v19, v18, 7 bitop3:0x6c
	v_xor_b32_e32 v26, v25, v22
	v_lshlrev_b32_e32 v142, 4, v18
	v_bitop3_b32 v18, v19, v23, 7 bitop3:0x6c
	v_lshlrev_b32_e32 v130, 7, v112
	v_and_b32_e32 v21, 8, v21
	v_lshlrev_b32_e32 v26, 4, v26
	v_lshlrev_b32_e32 v143, 4, v18
	v_lshrrev_b32_e32 v18, 3, v24
	v_or3_b32 v134, v26, v130, v21
	v_bitop3_b32 v26, v25, v22, 2 bitop3:0x36
	v_xor_b32_e32 v18, v18, v22
	v_lshlrev_b32_e32 v135, 4, v26
	v_bitop3_b32 v26, v25, v22, 4 bitop3:0x36
	v_lshlrev_b32_e32 v144, 4, v18
	v_lshlrev_b32_e32 v18, 1, v24
	v_lshlrev_b32_e32 v26, 4, v26
	v_and_or_b32 v145, v18, 8, v130
	v_lshrrev_b32_e32 v18, 3, v29
	v_or_b32_e32 v133, v21, v130
	v_bitop3_b32 v25, v25, v22, 6 bitop3:0x36
	v_add_lshl_u32 v141, v20, v112, 7
	v_xor_b32_e32 v18, v18, v22
	v_or3_b32 v147, v130, v26, v21
	v_mov_b32_e32 v20, v99
	v_mov_b32_e32 v21, v99
	v_lshlrev_b32_e32 v136, 4, v25
	v_lshlrev_b32_e32 v146, 4, v18
	v_mov_b32_e32 v18, v99
	v_mov_b32_e32 v19, v99
	v_mov_b32_e32 v50, 0
	v_mov_b64_e32 v[24:25], v[20:21]
	v_mov_b64_e32 v[28:29], v[20:21]
	v_mov_b64_e32 v[32:33], v[20:21]
	v_mov_b64_e32 v[36:37], v[20:21]
	v_mov_b64_e32 v[40:41], v[20:21]
	v_mov_b64_e32 v[44:45], v[20:21]
	v_mov_b64_e32 v[48:49], v[20:21]
	s_mov_b32 s26, 2
	v_add_u32_e32 v139, 8, v137
	s_movk_i32 s8, 0x1e40
	v_mov_b64_e32 v[22:23], v[18:19]
	v_mov_b64_e32 v[26:27], v[18:19]
	v_mov_b64_e32 v[30:31], v[18:19]
	v_mov_b64_e32 v[34:35], v[18:19]
	v_mov_b64_e32 v[38:39], v[18:19]
	v_mov_b64_e32 v[42:43], v[18:19]
	v_mov_b64_e32 v[46:47], v[18:19]
	v_mov_b32_e32 v51, v50
	v_mov_b32_e32 v52, v50
	v_mov_b32_e32 v53, v50
	v_mov_b32_e32 v54, v50
	v_mov_b32_e32 v55, v50
	v_mov_b32_e32 v56, v50
	v_mov_b32_e32 v57, v50
	s_cmpk_eq_i32 s8, 0x2140
	s_mov_b64 s[0:1], -1
	s_cbranch_scc1 .LBB0_386
